# baseline (speedup 1.0000x reference)
.LBB1_4:
	v_add_u32_e32 v182, s19, v191
	v_add_u32_e32 v238, s19, v192
	ds_read_b128 v[178:181], v182 offset:32768
	ds_read_b128 v[194:197], v182 offset:34816
	ds_read_b128 v[198:201], v182 offset:36864
	ds_read_b128 v[202:205], v182 offset:38912
	ds_read_b128 v[206:209], v238
	ds_read_b128 v[210:213], v238 offset:2048
	ds_read_b128 v[214:217], v238 offset:4096
	ds_read_b128 v[218:221], v238 offset:6144
	ds_read_b128 v[222:225], v238 offset:8192
	ds_read_b128 v[226:229], v238 offset:10240
	ds_read_b128 v[230:233], v238 offset:12288
	ds_read_b128 v[234:237], v238 offset:14336
	s_min_u32 s21, s20, 29
	s_xor_b32 s19, s19, 0x10000
	v_add_u32_e32 v239, s19, v189
	s_waitcnt vmcnt(11)
	v_cvt_pk_bf16_f32 v13, v12, v13
	v_cvt_pk_bf16_f32 v12, v10, v11
	s_waitcnt vmcnt(10)
	v_cvt_pk_bf16_f32 v11, v20, v21
	v_cvt_pk_bf16_f32 v10, v18, v19
	ds_write2st64_b64 v239, v[12:13], v[10:11] offset1:8
	s_waitcnt vmcnt(9)
	v_cvt_pk_bf16_f32 v11, v24, v25
	v_cvt_pk_bf16_f32 v10, v22, v23
	s_waitcnt vmcnt(8)
	v_cvt_pk_bf16_f32 v13, v32, v33
	v_cvt_pk_bf16_f32 v12, v30, v31
	ds_write2st64_b64 v239, v[10:11], v[12:13] offset0:16 offset1:24
	s_waitcnt vmcnt(7)
	v_cvt_pk_bf16_f32 v11, v36, v37
	v_cvt_pk_bf16_f32 v10, v34, v35
	s_waitcnt vmcnt(6)
	v_cvt_pk_bf16_f32 v13, v40, v41
	v_cvt_pk_bf16_f32 v12, v38, v39
	ds_write2st64_b64 v239, v[10:11], v[12:13] offset0:32 offset1:40
	s_waitcnt lgkmcnt(0)
	s_add_i32 s21, s21, 2
	s_barrier
	s_setprio 1
	s_waitcnt lgkmcnt(11)
	v_mfma_f32_16x16x32_bf16 v[174:177], v[178:181], v[206:209], v[174:177]
	s_lshl_b32 s22, s21, 1
	s_and_b32 s22, s22, 0x60
	s_add_i32 s22, s22, s12
	s_lshl_b32 s22, s22, 6
	v_mfma_f32_16x16x32_bf16 v[170:173], v[194:197], v[206:209], v[170:173]
	s_and_b32 s22, s22, 0x3f00
	s_or_b32 s22, s22, s13
	s_lshl_b32 s23, s21, 23
	s_lshl_b32 s22, s22, 9
	v_mfma_f32_16x16x32_bf16 v[158:161], v[198:201], v[206:209], v[158:161]
	s_and_b32 s23, s23, 0x7000000
	s_or_b32 s22, s22, s23
	s_lshl_b32 s23, s21, 8
	s_and_b32 s23, s23, 0x100
	s_or_b32 s22, s22, s23
	s_or_b32 s23, s22, 0x4000
	buffer_load_dwordx4 v[10:13], v1, s[4:7], s22 offen sc0 nt
	v_mfma_f32_16x16x32_bf16 v[142:145], v[202:205], v[206:209], v[142:145]
	s_waitcnt lgkmcnt(10)
	v_mfma_f32_16x16x32_bf16 v[166:169], v[178:181], v[210:213], v[166:169]
	v_mfma_f32_16x16x32_bf16 v[162:165], v[194:197], v[210:213], v[162:165]
	v_mfma_f32_16x16x32_bf16 v[146:149], v[198:201], v[210:213], v[146:149]
	buffer_load_dwordx4 v[18:21], v1, s[4:7], s23 offen sc0 nt
	s_or_b32 s23, s22, 0x8000
	v_mfma_f32_16x16x32_bf16 v[122:125], v[202:205], v[210:213], v[122:125]
	s_waitcnt lgkmcnt(9)
	v_mfma_f32_16x16x32_bf16 v[154:157], v[178:181], v[214:217], v[154:157]
	v_mfma_f32_16x16x32_bf16 v[150:153], v[194:197], v[214:217], v[150:153]
	v_mfma_f32_16x16x32_bf16 v[130:133], v[198:201], v[214:217], v[130:133]
	buffer_load_dwordx4 v[22:25], v1, s[4:7], s23 offen sc0 nt
	s_or_b32 s23, s22, 0xc000
	v_mfma_f32_16x16x32_bf16 v[106:109], v[202:205], v[214:217], v[106:109]
	s_waitcnt lgkmcnt(8)
	v_mfma_f32_16x16x32_bf16 v[138:141], v[178:181], v[218:221], v[138:141]
	v_mfma_f32_16x16x32_bf16 v[134:137], v[194:197], v[218:221], v[134:137]
	v_mfma_f32_16x16x32_bf16 v[114:117], v[198:201], v[218:221], v[114:117]
	buffer_load_dwordx4 v[30:33], v1, s[4:7], s23 offen sc0 nt
	s_or_b32 s23, s22, 0x10000
	v_mfma_f32_16x16x32_bf16 v[90:93], v[202:205], v[218:221], v[90:93]
	s_waitcnt lgkmcnt(7)
	v_mfma_f32_16x16x32_bf16 v[126:129], v[178:181], v[222:225], v[126:129]
	v_mfma_f32_16x16x32_bf16 v[118:121], v[194:197], v[222:225], v[118:121]
	v_mfma_f32_16x16x32_bf16 v[98:101], v[198:201], v[222:225], v[98:101]
	buffer_load_dwordx4 v[34:37], v1, s[4:7], s23 offen sc0 nt
	s_or_b32 s23, s22, 0x14000
	v_mfma_f32_16x16x32_bf16 v[74:77], v[202:205], v[222:225], v[74:77]
	s_waitcnt lgkmcnt(6)
	v_mfma_f32_16x16x32_bf16 v[110:113], v[178:181], v[226:229], v[110:113]
	v_mfma_f32_16x16x32_bf16 v[102:105], v[194:197], v[226:229], v[102:105]
	v_mfma_f32_16x16x32_bf16 v[82:85], v[198:201], v[226:229], v[82:85]
	buffer_load_dwordx4 v[38:41], v1, s[4:7], s23 offen sc0 nt
	s_or_b32 s27, s22, 0x18000
	s_or_b32 s28, s22, 0x1c000
	v_mfma_f32_16x16x32_bf16 v[62:65], v[202:205], v[226:229], v[62:65]
	s_waitcnt lgkmcnt(5)
	v_mfma_f32_16x16x32_bf16 v[94:97], v[178:181], v[230:233], v[94:97]
	v_mfma_f32_16x16x32_bf16 v[86:89], v[194:197], v[230:233], v[86:89]
	v_mfma_f32_16x16x32_bf16 v[70:73], v[198:201], v[230:233], v[70:73]
	v_mfma_f32_16x16x32_bf16 v[54:57], v[202:205], v[230:233], v[54:57]
	s_waitcnt lgkmcnt(4)
	v_mfma_f32_16x16x32_bf16 v[78:81], v[178:181], v[234:237], v[78:81]
	v_mfma_f32_16x16x32_bf16 v[66:69], v[194:197], v[234:237], v[66:69]
	v_mfma_f32_16x16x32_bf16 v[58:61], v[198:201], v[234:237], v[58:61]
	v_mfma_f32_16x16x32_bf16 v[50:53], v[202:205], v[234:237], v[50:53]
	s_setprio 0
	s_waitcnt lgkmcnt(0)
	s_barrier
	ds_read_b128 v[178:181], v182 offset:33792
	ds_read_b128 v[194:197], v182 offset:35840
	ds_read_b128 v[198:201], v182 offset:37888
	ds_read_b128 v[202:205], v182 offset:39936
	ds_read_b128 v[206:209], v238 offset:1024
	ds_read_b128 v[210:213], v238 offset:3072
	ds_read_b128 v[214:217], v238 offset:5120
	ds_read_b128 v[218:221], v238 offset:7168
	ds_read_b128 v[222:225], v238 offset:9216
	ds_read_b128 v[226:229], v238 offset:11264
	ds_read_b128 v[230:233], v238 offset:13312
	ds_read_b128 v[234:237], v238 offset:15360
	v_add_u32_e32 v182, s19, v190
	s_waitcnt vmcnt(11)
	v_cvt_pk_bf16_f32 v42, v42, v43
	v_cvt_pk_bf16_f32 v43, v44, v45
	s_waitcnt vmcnt(9)
	v_cvt_pk_bf16_f32 v46, v46, v47
	v_cvt_pk_bf16_f32 v47, v48, v49
	ds_write2st64_b64 v239, v[42:43], v[46:47] offset0:48 offset1:56
	s_waitcnt vmcnt(9)
	ds_write_b128 v182, v[2:5] offset:32768
	s_waitcnt vmcnt(8)
	ds_write_b128 v182, v[6:9] offset:40960
	s_waitcnt vmcnt(7)
	ds_write_b128 v182, v[14:17] offset:49152
	s_waitcnt vmcnt(6)
	ds_write_b128 v182, v[26:29] offset:57344
	s_waitcnt lgkmcnt(0)
	s_barrier
	s_setprio 1
	s_waitcnt lgkmcnt(11)
	v_mfma_f32_16x16x32_bf16 v[174:177], v[178:181], v[206:209], v[174:177]
	s_lshl_b32 s21, s21, 7
	s_and_b32 s21, s21, 0x780
	s_or_b32 s21, s21, s14
	s_or_b32 s22, s21, 0x20000
	v_mfma_f32_16x16x32_bf16 v[170:173], v[194:197], v[206:209], v[170:173]
	v_mfma_f32_16x16x32_bf16 v[158:161], v[198:201], v[206:209], v[158:161]
	buffer_load_dwordx4 v[42:45], v1, s[4:7], s27 offen sc0 nt
	v_mfma_f32_16x16x32_bf16 v[142:145], v[202:205], v[206:209], v[142:145]
	s_waitcnt lgkmcnt(10)
	v_mfma_f32_16x16x32_bf16 v[166:169], v[178:181], v[210:213], v[166:169]
	v_mfma_f32_16x16x32_bf16 v[162:165], v[194:197], v[210:213], v[162:165]
	buffer_load_dwordx4 v[2:5], v188, s[0:3], s21 offen sc1
	v_mfma_f32_16x16x32_bf16 v[146:149], v[198:201], v[210:213], v[146:149]
	v_mfma_f32_16x16x32_bf16 v[122:125], v[202:205], v[210:213], v[122:125]
	s_waitcnt lgkmcnt(9)
	v_mfma_f32_16x16x32_bf16 v[154:157], v[178:181], v[214:217], v[154:157]
	v_mfma_f32_16x16x32_bf16 v[150:153], v[194:197], v[214:217], v[150:153]
	v_mfma_f32_16x16x32_bf16 v[130:133], v[198:201], v[214:217], v[130:133]
	buffer_load_dwordx4 v[46:49], v1, s[4:7], s28 offen sc0 nt
	v_mfma_f32_16x16x32_bf16 v[106:109], v[202:205], v[214:217], v[106:109]
	s_waitcnt lgkmcnt(8)
	v_mfma_f32_16x16x32_bf16 v[138:141], v[178:181], v[218:221], v[138:141]
	v_mfma_f32_16x16x32_bf16 v[134:137], v[194:197], v[218:221], v[134:137]
	buffer_load_dwordx4 v[6:9], v188, s[0:3], s22 offen sc1
	s_or_b32 s22, s21, 0x40000
	s_or_b32 s21, s21, 0x60000
	v_mfma_f32_16x16x32_bf16 v[114:117], v[198:201], v[218:221], v[114:117]
	v_mfma_f32_16x16x32_bf16 v[90:93], v[202:205], v[218:221], v[90:93]
	s_waitcnt lgkmcnt(7)
	v_mfma_f32_16x16x32_bf16 v[126:129], v[178:181], v[222:225], v[126:129]
	v_mfma_f32_16x16x32_bf16 v[118:121], v[194:197], v[222:225], v[118:121]
	v_mfma_f32_16x16x32_bf16 v[98:101], v[198:201], v[222:225], v[98:101]
	v_mfma_f32_16x16x32_bf16 v[74:77], v[202:205], v[222:225], v[74:77]
	s_waitcnt lgkmcnt(6)
	v_mfma_f32_16x16x32_bf16 v[110:113], v[178:181], v[226:229], v[110:113]
	v_mfma_f32_16x16x32_bf16 v[102:105], v[194:197], v[226:229], v[102:105]
	buffer_load_dwordx4 v[14:17], v188, s[0:3], s22 offen sc1
	v_mfma_f32_16x16x32_bf16 v[82:85], v[198:201], v[226:229], v[82:85]
	v_mfma_f32_16x16x32_bf16 v[62:65], v[202:205], v[226:229], v[62:65]
	s_waitcnt lgkmcnt(5)
	v_mfma_f32_16x16x32_bf16 v[94:97], v[178:181], v[230:233], v[94:97]
	v_mfma_f32_16x16x32_bf16 v[86:89], v[194:197], v[230:233], v[86:89]
	v_mfma_f32_16x16x32_bf16 v[70:73], v[198:201], v[230:233], v[70:73]
	v_mfma_f32_16x16x32_bf16 v[54:57], v[202:205], v[230:233], v[54:57]
	s_waitcnt lgkmcnt(4)
	v_mfma_f32_16x16x32_bf16 v[78:81], v[178:181], v[234:237], v[78:81]
	v_mfma_f32_16x16x32_bf16 v[66:69], v[194:197], v[234:237], v[66:69]
	buffer_load_dwordx4 v[26:29], v188, s[0:3], s21 offen sc1
	v_mfma_f32_16x16x32_bf16 v[58:61], v[198:201], v[234:237], v[58:61]
	v_mfma_f32_16x16x32_bf16 v[50:53], v[202:205], v[234:237], v[50:53]
	s_setprio 0
	s_and_b32 s21, s20, 15
	s_cmp_lg_u32 s21, 15
	s_cbranch_scc1 .LBB1_3
	s_and_b32 s21, s18, 32
	s_add_i32 s21, s21, s12
	s_lshl_b32 s21, s21, 6
	s_and_b32 s21, s21, 0x3f00
	v_add_lshl_u32 v182, v193, s21, 9
	v_lshl_add_u64 v[206:207], v[184:185], 0, v[182:183]
	v_add_co_u32_e32 v208, vcc, s8, v206
	s_nop 1
	v_addc_co_u32_e32 v209, vcc, 0, v207, vcc
	v_add_co_u32_e32 v210, vcc, s15, v206
	s_nop 1
	v_addc_co_u32_e32 v211, vcc, 0, v207, vcc
	v_add_co_u32_e32 v212, vcc, s9, v206
	s_nop 1
	v_addc_co_u32_e32 v213, vcc, 0, v207, vcc
	v_add_co_u32_e32 v214, vcc, s16, v206
	s_nop 1
	v_addc_co_u32_e32 v215, vcc, 0, v207, vcc
	v_add_co_u32_e32 v216, vcc, s10, v206
	s_nop 1
	v_addc_co_u32_e32 v217, vcc, 0, v207, vcc
	v_add_co_u32_e32 v218, vcc, s17, v206
	s_nop 1
	v_addc_co_u32_e32 v219, vcc, 0, v207, vcc
	v_add_co_u32_e32 v220, vcc, s11, v206
	s_nop 1
	v_addc_co_u32_e32 v221, vcc, 0, v207, vcc
	global_store_dwordx4 v[206:207], v[174:177], off
	global_store_dwordx4 v[206:207], v[170:173], off offset:64
	global_store_dwordx4 v[206:207], v[158:161], off offset:128
	global_store_dwordx4 v[206:207], v[142:145], off offset:192
	global_store_dwordx4 v[208:209], v[166:169], off
	global_store_dwordx4 v[208:209], v[162:165], off offset:64
	global_store_dwordx4 v[208:209], v[146:149], off offset:128
	global_store_dwordx4 v[208:209], v[122:125], off offset:192
	global_store_dwordx4 v[210:211], v[154:157], off
	global_store_dwordx4 v[210:211], v[150:153], off offset:64
	global_store_dwordx4 v[210:211], v[130:133], off offset:128
	global_store_dwordx4 v[210:211], v[106:109], off offset:192
	global_store_dwordx4 v[212:213], v[138:141], off
	global_store_dwordx4 v[212:213], v[134:137], off offset:64
	global_store_dwordx4 v[212:213], v[114:117], off offset:128
	global_store_dwordx4 v[212:213], v[90:93], off offset:192
	global_store_dwordx4 v[214:215], v[126:129], off
	global_store_dwordx4 v[214:215], v[118:121], off offset:64
	global_store_dwordx4 v[214:215], v[98:101], off offset:128
	global_store_dwordx4 v[214:215], v[74:77], off offset:192
	global_store_dwordx4 v[216:217], v[110:113], off
	global_store_dwordx4 v[216:217], v[102:105], off offset:64
	global_store_dwordx4 v[216:217], v[82:85], off offset:128
	global_store_dwordx4 v[216:217], v[62:65], off offset:192
	global_store_dwordx4 v[218:219], v[94:97], off
	global_store_dwordx4 v[218:219], v[86:89], off offset:64
	global_store_dwordx4 v[218:219], v[70:73], off offset:128
	global_store_dwordx4 v[218:219], v[54:57], off offset:192
	global_store_dwordx4 v[220:221], v[78:81], off
	global_store_dwordx4 v[220:221], v[66:69], off offset:64
	global_store_dwordx4 v[220:221], v[58:61], off offset:128
	global_store_dwordx4 v[220:221], v[50:53], off offset:192
.Lpd_tail:
	s_waitcnt lgkmcnt(0)
	s_barrier
	s_add_i32 s20, s20, 1
	s_add_i32 s18, s18, 2
	v_add_u32_e32 v182, s19, v191
	v_add_u32_e32 v238, s19, v192
	ds_read_b128 v[178:181], v182 offset:32768
	ds_read_b128 v[194:197], v182 offset:34816
	ds_read_b128 v[198:201], v182 offset:36864
	ds_read_b128 v[202:205], v182 offset:38912
	ds_read_b128 v[206:209], v238
	ds_read_b128 v[210:213], v238 offset:2048
	ds_read_b128 v[214:217], v238 offset:4096
	ds_read_b128 v[218:221], v238 offset:6144
	ds_read_b128 v[222:225], v238 offset:8192
	ds_read_b128 v[226:229], v238 offset:10240
	ds_read_b128 v[230:233], v238 offset:12288
	ds_read_b128 v[234:237], v238 offset:14336
	s_min_u32 s21, s20, 29
	s_xor_b32 s19, s19, 0x10000
	v_add_u32_e32 v239, s19, v189
	s_waitcnt vmcnt(43)
	v_cvt_pk_bf16_f32 v13, v12, v13
	v_cvt_pk_bf16_f32 v12, v10, v11
	s_waitcnt vmcnt(42)
	v_cvt_pk_bf16_f32 v11, v20, v21
	v_cvt_pk_bf16_f32 v10, v18, v19
	ds_write2st64_b64 v239, v[12:13], v[10:11] offset1:8
	s_waitcnt vmcnt(41)
	v_cvt_pk_bf16_f32 v11, v24, v25
	v_cvt_pk_bf16_f32 v10, v22, v23
	s_waitcnt vmcnt(40)
	v_cvt_pk_bf16_f32 v13, v32, v33
	v_cvt_pk_bf16_f32 v12, v30, v31
	ds_write2st64_b64 v239, v[10:11], v[12:13] offset0:16 offset1:24
	s_waitcnt vmcnt(39)
	v_cvt_pk_bf16_f32 v11, v36, v37
	v_cvt_pk_bf16_f32 v10, v34, v35
	s_waitcnt vmcnt(38)
	v_cvt_pk_bf16_f32 v13, v40, v41
	v_cvt_pk_bf16_f32 v12, v38, v39
	ds_write2st64_b64 v239, v[10:11], v[12:13] offset0:32 offset1:40
	s_waitcnt lgkmcnt(0)
	s_add_i32 s21, s21, 2
	s_barrier
	s_setprio 1
	s_waitcnt lgkmcnt(11)
	v_mfma_f32_16x16x32_bf16 v[174:177], v[178:181], v[206:209], v[240:243]
	s_lshl_b32 s22, s21, 1
	s_and_b32 s22, s22, 0x60
	s_add_i32 s22, s22, s12
	s_lshl_b32 s22, s22, 6
	v_mfma_f32_16x16x32_bf16 v[170:173], v[194:197], v[206:209], v[244:247]
	s_and_b32 s22, s22, 0x3f00
	s_or_b32 s22, s22, s13
	s_lshl_b32 s23, s21, 23
	s_lshl_b32 s22, s22, 9
	v_mfma_f32_16x16x32_bf16 v[158:161], v[198:201], v[206:209], v[248:251]
	s_and_b32 s23, s23, 0x7000000
	s_or_b32 s22, s22, s23
	s_lshl_b32 s23, s21, 8
	s_and_b32 s23, s23, 0x100
	s_or_b32 s22, s22, s23
	s_or_b32 s23, s22, 0x4000
	buffer_load_dwordx4 v[10:13], v1, s[4:7], s22 offen sc0 nt
	v_mfma_f32_16x16x32_bf16 v[142:145], v[202:205], v[206:209], v[252:255]
	s_waitcnt lgkmcnt(10)
	v_mfma_f32_16x16x32_bf16 v[166:169], v[178:181], v[210:213], v[240:243]
	v_mfma_f32_16x16x32_bf16 v[162:165], v[194:197], v[210:213], v[244:247]
	v_mfma_f32_16x16x32_bf16 v[146:149], v[198:201], v[210:213], v[248:251]
	buffer_load_dwordx4 v[18:21], v1, s[4:7], s23 offen sc0 nt
	s_or_b32 s23, s22, 0x8000
	v_mfma_f32_16x16x32_bf16 v[122:125], v[202:205], v[210:213], v[252:255]
	s_waitcnt lgkmcnt(9)
	v_mfma_f32_16x16x32_bf16 v[154:157], v[178:181], v[214:217], v[240:243]
	v_mfma_f32_16x16x32_bf16 v[150:153], v[194:197], v[214:217], v[244:247]
	v_mfma_f32_16x16x32_bf16 v[130:133], v[198:201], v[214:217], v[248:251]
	buffer_load_dwordx4 v[22:25], v1, s[4:7], s23 offen sc0 nt
	s_or_b32 s23, s22, 0xc000
	v_mfma_f32_16x16x32_bf16 v[106:109], v[202:205], v[214:217], v[252:255]
	s_waitcnt lgkmcnt(8)
	v_mfma_f32_16x16x32_bf16 v[138:141], v[178:181], v[218:221], v[240:243]
	v_mfma_f32_16x16x32_bf16 v[134:137], v[194:197], v[218:221], v[244:247]
	v_mfma_f32_16x16x32_bf16 v[114:117], v[198:201], v[218:221], v[248:251]
	buffer_load_dwordx4 v[30:33], v1, s[4:7], s23 offen sc0 nt
	s_or_b32 s23, s22, 0x10000
	v_mfma_f32_16x16x32_bf16 v[90:93], v[202:205], v[218:221], v[252:255]
	s_waitcnt lgkmcnt(7)
	v_mfma_f32_16x16x32_bf16 v[126:129], v[178:181], v[222:225], v[240:243]
	v_mfma_f32_16x16x32_bf16 v[118:121], v[194:197], v[222:225], v[244:247]
	v_mfma_f32_16x16x32_bf16 v[98:101], v[198:201], v[222:225], v[248:251]
	buffer_load_dwordx4 v[34:37], v1, s[4:7], s23 offen sc0 nt
	s_or_b32 s23, s22, 0x14000
	v_mfma_f32_16x16x32_bf16 v[74:77], v[202:205], v[222:225], v[252:255]
	s_waitcnt lgkmcnt(6)
	v_mfma_f32_16x16x32_bf16 v[110:113], v[178:181], v[226:229], v[240:243]
	v_mfma_f32_16x16x32_bf16 v[102:105], v[194:197], v[226:229], v[244:247]
	v_mfma_f32_16x16x32_bf16 v[82:85], v[198:201], v[226:229], v[248:251]
	buffer_load_dwordx4 v[38:41], v1, s[4:7], s23 offen sc0 nt
	s_or_b32 s27, s22, 0x18000
	s_or_b32 s28, s22, 0x1c000
	v_mfma_f32_16x16x32_bf16 v[62:65], v[202:205], v[226:229], v[252:255]
	s_waitcnt lgkmcnt(5)
	v_mfma_f32_16x16x32_bf16 v[94:97], v[178:181], v[230:233], v[240:243]
	v_mfma_f32_16x16x32_bf16 v[86:89], v[194:197], v[230:233], v[244:247]
	v_mfma_f32_16x16x32_bf16 v[70:73], v[198:201], v[230:233], v[248:251]
	v_mfma_f32_16x16x32_bf16 v[54:57], v[202:205], v[230:233], v[252:255]
	s_waitcnt lgkmcnt(4)
	v_mfma_f32_16x16x32_bf16 v[78:81], v[178:181], v[234:237], v[240:243]
	v_mfma_f32_16x16x32_bf16 v[66:69], v[194:197], v[234:237], v[244:247]
	v_mfma_f32_16x16x32_bf16 v[58:61], v[198:201], v[234:237], v[248:251]
	v_mfma_f32_16x16x32_bf16 v[50:53], v[202:205], v[234:237], v[252:255]
	s_setprio 0
	s_waitcnt lgkmcnt(0)
	s_barrier
	ds_read_b128 v[178:181], v182 offset:33792
	ds_read_b128 v[194:197], v182 offset:35840
	ds_read_b128 v[198:201], v182 offset:37888
	ds_read_b128 v[202:205], v182 offset:39936
	ds_read_b128 v[206:209], v238 offset:1024
	ds_read_b128 v[210:213], v238 offset:3072
	ds_read_b128 v[214:217], v238 offset:5120
	ds_read_b128 v[218:221], v238 offset:7168
	ds_read_b128 v[222:225], v238 offset:9216
	ds_read_b128 v[226:229], v238 offset:11264
	ds_read_b128 v[230:233], v238 offset:13312
	ds_read_b128 v[234:237], v238 offset:15360
	v_add_u32_e32 v182, s19, v190
	s_waitcnt vmcnt(43)
	v_cvt_pk_bf16_f32 v42, v42, v43
	v_cvt_pk_bf16_f32 v43, v44, v45
	s_waitcnt vmcnt(41)
	v_cvt_pk_bf16_f32 v46, v46, v47
	v_cvt_pk_bf16_f32 v47, v48, v49
	ds_write2st64_b64 v239, v[42:43], v[46:47] offset0:48 offset1:56
	s_waitcnt vmcnt(41)
	ds_write_b128 v182, v[2:5] offset:32768
	s_waitcnt vmcnt(40)
	ds_write_b128 v182, v[6:9] offset:40960
	s_waitcnt vmcnt(39)
	ds_write_b128 v182, v[14:17] offset:49152
	s_waitcnt vmcnt(38)
	ds_write_b128 v182, v[26:29] offset:57344
	s_waitcnt lgkmcnt(0)
	s_barrier
	s_setprio 1
	s_waitcnt lgkmcnt(11)
	v_mfma_f32_16x16x32_bf16 v[174:177], v[178:181], v[206:209], v[174:177]
	s_lshl_b32 s21, s21, 7
	s_and_b32 s21, s21, 0x780
	s_or_b32 s21, s21, s14
	s_or_b32 s22, s21, 0x20000
	v_mfma_f32_16x16x32_bf16 v[170:173], v[194:197], v[206:209], v[170:173]
	v_mfma_f32_16x16x32_bf16 v[158:161], v[198:201], v[206:209], v[158:161]
	buffer_load_dwordx4 v[42:45], v1, s[4:7], s27 offen sc0 nt
	v_mfma_f32_16x16x32_bf16 v[142:145], v[202:205], v[206:209], v[142:145]
	s_waitcnt lgkmcnt(10)
	v_mfma_f32_16x16x32_bf16 v[166:169], v[178:181], v[210:213], v[166:169]
	v_mfma_f32_16x16x32_bf16 v[162:165], v[194:197], v[210:213], v[162:165]
	buffer_load_dwordx4 v[2:5], v188, s[0:3], s21 offen sc1
	v_mfma_f32_16x16x32_bf16 v[146:149], v[198:201], v[210:213], v[146:149]
	v_mfma_f32_16x16x32_bf16 v[122:125], v[202:205], v[210:213], v[122:125]
	s_waitcnt lgkmcnt(9)
	v_mfma_f32_16x16x32_bf16 v[154:157], v[178:181], v[214:217], v[154:157]
	v_mfma_f32_16x16x32_bf16 v[150:153], v[194:197], v[214:217], v[150:153]
	v_mfma_f32_16x16x32_bf16 v[130:133], v[198:201], v[214:217], v[130:133]
	buffer_load_dwordx4 v[46:49], v1, s[4:7], s28 offen sc0 nt
	v_mfma_f32_16x16x32_bf16 v[106:109], v[202:205], v[214:217], v[106:109]
	s_waitcnt lgkmcnt(8)
	v_mfma_f32_16x16x32_bf16 v[138:141], v[178:181], v[218:221], v[138:141]
	v_mfma_f32_16x16x32_bf16 v[134:137], v[194:197], v[218:221], v[134:137]
	buffer_load_dwordx4 v[6:9], v188, s[0:3], s22 offen sc1
	s_or_b32 s22, s21, 0x40000
	s_or_b32 s21, s21, 0x60000
	v_mfma_f32_16x16x32_bf16 v[114:117], v[198:201], v[218:221], v[114:117]
	v_mfma_f32_16x16x32_bf16 v[90:93], v[202:205], v[218:221], v[90:93]
	s_waitcnt lgkmcnt(7)
	v_mfma_f32_16x16x32_bf16 v[126:129], v[178:181], v[222:225], v[126:129]
	v_mfma_f32_16x16x32_bf16 v[118:121], v[194:197], v[222:225], v[118:121]
	v_mfma_f32_16x16x32_bf16 v[98:101], v[198:201], v[222:225], v[98:101]
	v_mfma_f32_16x16x32_bf16 v[74:77], v[202:205], v[222:225], v[74:77]
	s_waitcnt lgkmcnt(6)
	v_mfma_f32_16x16x32_bf16 v[110:113], v[178:181], v[226:229], v[110:113]
	v_mfma_f32_16x16x32_bf16 v[102:105], v[194:197], v[226:229], v[102:105]
	buffer_load_dwordx4 v[14:17], v188, s[0:3], s22 offen sc1
	v_mfma_f32_16x16x32_bf16 v[82:85], v[198:201], v[226:229], v[82:85]
	v_mfma_f32_16x16x32_bf16 v[62:65], v[202:205], v[226:229], v[62:65]
	s_waitcnt lgkmcnt(5)
	v_mfma_f32_16x16x32_bf16 v[94:97], v[178:181], v[230:233], v[94:97]
	v_mfma_f32_16x16x32_bf16 v[86:89], v[194:197], v[230:233], v[86:89]
	v_mfma_f32_16x16x32_bf16 v[70:73], v[198:201], v[230:233], v[70:73]
	v_mfma_f32_16x16x32_bf16 v[54:57], v[202:205], v[230:233], v[54:57]
	s_waitcnt lgkmcnt(4)
	v_mfma_f32_16x16x32_bf16 v[78:81], v[178:181], v[234:237], v[78:81]
	v_mfma_f32_16x16x32_bf16 v[66:69], v[194:197], v[234:237], v[66:69]
	buffer_load_dwordx4 v[26:29], v188, s[0:3], s21 offen sc1
	v_mfma_f32_16x16x32_bf16 v[58:61], v[198:201], v[234:237], v[58:61]
	v_mfma_f32_16x16x32_bf16 v[50:53], v[202:205], v[234:237], v[50:53]
	s_setprio 0
	s_branch .LBB1_3
.Lt30:
	v_add_u32_e32 v182, s19, v191
	v_add_u32_e32 v238, s19, v192
	ds_read_b128 v[178:181], v182 offset:32768
	ds_read_b128 v[194:197], v182 offset:34816
	ds_read_b128 v[198:201], v182 offset:36864
	ds_read_b128 v[202:205], v182 offset:38912
	ds_read_b128 v[206:209], v238
	ds_read_b128 v[210:213], v238 offset:2048
	ds_read_b128 v[214:217], v238 offset:4096
	ds_read_b128 v[218:221], v238 offset:6144
	ds_read_b128 v[222:225], v238 offset:8192
	ds_read_b128 v[226:229], v238 offset:10240
	ds_read_b128 v[230:233], v238 offset:12288
	ds_read_b128 v[234:237], v238 offset:14336
	s_min_u32 s21, s20, 29
	s_xor_b32 s19, s19, 0x10000
	v_add_u32_e32 v239, s19, v189
	s_waitcnt vmcnt(11)
	v_cvt_pk_bf16_f32 v13, v12, v13
	v_cvt_pk_bf16_f32 v12, v10, v11
	s_waitcnt vmcnt(10)
	v_cvt_pk_bf16_f32 v11, v20, v21
	v_cvt_pk_bf16_f32 v10, v18, v19
	ds_write2st64_b64 v239, v[12:13], v[10:11] offset1:8
	s_waitcnt vmcnt(9)
	v_cvt_pk_bf16_f32 v11, v24, v25
	v_cvt_pk_bf16_f32 v10, v22, v23
	s_waitcnt vmcnt(8)
	v_cvt_pk_bf16_f32 v13, v32, v33
	v_cvt_pk_bf16_f32 v12, v30, v31
	ds_write2st64_b64 v239, v[10:11], v[12:13] offset0:16 offset1:24
	s_waitcnt vmcnt(7)
	v_cvt_pk_bf16_f32 v11, v36, v37
	v_cvt_pk_bf16_f32 v10, v34, v35
	s_waitcnt vmcnt(6)
	v_cvt_pk_bf16_f32 v13, v40, v41
	v_cvt_pk_bf16_f32 v12, v38, v39
	ds_write2st64_b64 v239, v[10:11], v[12:13] offset0:32 offset1:40
	s_waitcnt lgkmcnt(0)
	s_add_i32 s21, s21, 2
	s_barrier
	s_setprio 1
	s_waitcnt lgkmcnt(11)
	v_mfma_f32_16x16x32_bf16 v[174:177], v[178:181], v[206:209], v[174:177]
	s_lshl_b32 s22, s21, 1
	s_and_b32 s22, s22, 0x60
	s_add_i32 s22, s22, s12
	s_lshl_b32 s22, s22, 6
	v_mfma_f32_16x16x32_bf16 v[170:173], v[194:197], v[206:209], v[170:173]
	s_and_b32 s22, s22, 0x3f00
	s_or_b32 s22, s22, s13
	s_lshl_b32 s23, s21, 23
	s_lshl_b32 s22, s22, 9
	v_mfma_f32_16x16x32_bf16 v[158:161], v[198:201], v[206:209], v[158:161]
	s_and_b32 s23, s23, 0x7000000
	s_or_b32 s22, s22, s23
	s_lshl_b32 s23, s21, 8
	s_and_b32 s23, s23, 0x100
	s_or_b32 s22, s22, s23
	s_or_b32 s23, s22, 0x4000
	v_mfma_f32_16x16x32_bf16 v[142:145], v[202:205], v[206:209], v[142:145]
	s_waitcnt lgkmcnt(10)
	v_mfma_f32_16x16x32_bf16 v[166:169], v[178:181], v[210:213], v[166:169]
	v_mfma_f32_16x16x32_bf16 v[162:165], v[194:197], v[210:213], v[162:165]
	v_mfma_f32_16x16x32_bf16 v[146:149], v[198:201], v[210:213], v[146:149]
	s_or_b32 s23, s22, 0x8000
	v_mfma_f32_16x16x32_bf16 v[122:125], v[202:205], v[210:213], v[122:125]
	s_waitcnt lgkmcnt(9)
	v_mfma_f32_16x16x32_bf16 v[154:157], v[178:181], v[214:217], v[154:157]
	v_mfma_f32_16x16x32_bf16 v[150:153], v[194:197], v[214:217], v[150:153]
	v_mfma_f32_16x16x32_bf16 v[130:133], v[198:201], v[214:217], v[130:133]
	s_or_b32 s23, s22, 0xc000
	v_mfma_f32_16x16x32_bf16 v[106:109], v[202:205], v[214:217], v[106:109]
	s_waitcnt lgkmcnt(8)
	v_mfma_f32_16x16x32_bf16 v[138:141], v[178:181], v[218:221], v[138:141]
	v_mfma_f32_16x16x32_bf16 v[134:137], v[194:197], v[218:221], v[134:137]
	v_mfma_f32_16x16x32_bf16 v[114:117], v[198:201], v[218:221], v[114:117]
	s_or_b32 s23, s22, 0x10000
	v_mfma_f32_16x16x32_bf16 v[90:93], v[202:205], v[218:221], v[90:93]
	s_waitcnt lgkmcnt(7)
	v_mfma_f32_16x16x32_bf16 v[126:129], v[178:181], v[222:225], v[126:129]
	v_mfma_f32_16x16x32_bf16 v[118:121], v[194:197], v[222:225], v[118:121]
	v_mfma_f32_16x16x32_bf16 v[98:101], v[198:201], v[222:225], v[98:101]
	s_or_b32 s23, s22, 0x14000
	v_mfma_f32_16x16x32_bf16 v[74:77], v[202:205], v[222:225], v[74:77]
	s_waitcnt lgkmcnt(6)
	v_mfma_f32_16x16x32_bf16 v[110:113], v[178:181], v[226:229], v[110:113]
	v_mfma_f32_16x16x32_bf16 v[102:105], v[194:197], v[226:229], v[102:105]
	v_mfma_f32_16x16x32_bf16 v[82:85], v[198:201], v[226:229], v[82:85]
	s_or_b32 s27, s22, 0x18000
	s_or_b32 s28, s22, 0x1c000
	v_mfma_f32_16x16x32_bf16 v[62:65], v[202:205], v[226:229], v[62:65]
	s_waitcnt lgkmcnt(5)
	v_mfma_f32_16x16x32_bf16 v[94:97], v[178:181], v[230:233], v[94:97]
	v_mfma_f32_16x16x32_bf16 v[86:89], v[194:197], v[230:233], v[86:89]
	v_mfma_f32_16x16x32_bf16 v[70:73], v[198:201], v[230:233], v[70:73]
	v_mfma_f32_16x16x32_bf16 v[54:57], v[202:205], v[230:233], v[54:57]
	s_waitcnt lgkmcnt(4)
	v_mfma_f32_16x16x32_bf16 v[78:81], v[178:181], v[234:237], v[78:81]
	v_mfma_f32_16x16x32_bf16 v[66:69], v[194:197], v[234:237], v[66:69]
	v_mfma_f32_16x16x32_bf16 v[58:61], v[198:201], v[234:237], v[58:61]
	v_mfma_f32_16x16x32_bf16 v[50:53], v[202:205], v[234:237], v[50:53]
	s_setprio 0
	s_waitcnt lgkmcnt(0)
	s_barrier
	ds_read_b128 v[178:181], v182 offset:33792
	ds_read_b128 v[194:197], v182 offset:35840
	ds_read_b128 v[198:201], v182 offset:37888
	ds_read_b128 v[202:205], v182 offset:39936
	ds_read_b128 v[206:209], v238 offset:1024
	ds_read_b128 v[210:213], v238 offset:3072
	ds_read_b128 v[214:217], v238 offset:5120
	ds_read_b128 v[218:221], v238 offset:7168
	ds_read_b128 v[222:225], v238 offset:9216
	ds_read_b128 v[226:229], v238 offset:11264
	ds_read_b128 v[230:233], v238 offset:13312
	ds_read_b128 v[234:237], v238 offset:15360
	v_add_u32_e32 v182, s19, v190
	s_waitcnt vmcnt(5)
	v_cvt_pk_bf16_f32 v42, v42, v43
	v_cvt_pk_bf16_f32 v43, v44, v45
	s_waitcnt vmcnt(3)
	v_cvt_pk_bf16_f32 v46, v46, v47
	v_cvt_pk_bf16_f32 v47, v48, v49
	ds_write2st64_b64 v239, v[42:43], v[46:47] offset0:48 offset1:56
	s_waitcnt vmcnt(3)
	ds_write_b128 v182, v[2:5] offset:32768
	s_waitcnt vmcnt(2)
	ds_write_b128 v182, v[6:9] offset:40960
	s_waitcnt vmcnt(1)
	ds_write_b128 v182, v[14:17] offset:49152
	s_waitcnt vmcnt(0)
	ds_write_b128 v182, v[26:29] offset:57344
	s_waitcnt lgkmcnt(0)
	s_barrier
	s_setprio 1
	s_waitcnt lgkmcnt(11)
	v_mfma_f32_16x16x32_bf16 v[174:177], v[178:181], v[206:209], v[174:177]
	s_lshl_b32 s21, s21, 7
	s_and_b32 s21, s21, 0x780
	s_or_b32 s21, s21, s14
	s_or_b32 s22, s21, 0x20000
	v_mfma_f32_16x16x32_bf16 v[170:173], v[194:197], v[206:209], v[170:173]
	v_mfma_f32_16x16x32_bf16 v[158:161], v[198:201], v[206:209], v[158:161]
	v_mfma_f32_16x16x32_bf16 v[142:145], v[202:205], v[206:209], v[142:145]
	s_waitcnt lgkmcnt(10)
	v_mfma_f32_16x16x32_bf16 v[166:169], v[178:181], v[210:213], v[166:169]
	v_mfma_f32_16x16x32_bf16 v[162:165], v[194:197], v[210:213], v[162:165]
	v_mfma_f32_16x16x32_bf16 v[146:149], v[198:201], v[210:213], v[146:149]
	v_mfma_f32_16x16x32_bf16 v[122:125], v[202:205], v[210:213], v[122:125]
	s_waitcnt lgkmcnt(9)
	v_mfma_f32_16x16x32_bf16 v[154:157], v[178:181], v[214:217], v[154:157]
	v_mfma_f32_16x16x32_bf16 v[150:153], v[194:197], v[214:217], v[150:153]
	v_mfma_f32_16x16x32_bf16 v[130:133], v[198:201], v[214:217], v[130:133]
	v_mfma_f32_16x16x32_bf16 v[106:109], v[202:205], v[214:217], v[106:109]
	s_waitcnt lgkmcnt(8)
	v_mfma_f32_16x16x32_bf16 v[138:141], v[178:181], v[218:221], v[138:141]
	v_mfma_f32_16x16x32_bf16 v[134:137], v[194:197], v[218:221], v[134:137]
	s_or_b32 s22, s21, 0x40000
	s_or_b32 s21, s21, 0x60000
	v_mfma_f32_16x16x32_bf16 v[114:117], v[198:201], v[218:221], v[114:117]
	v_mfma_f32_16x16x32_bf16 v[90:93], v[202:205], v[218:221], v[90:93]
	s_waitcnt lgkmcnt(7)
	v_mfma_f32_16x16x32_bf16 v[126:129], v[178:181], v[222:225], v[126:129]
	v_mfma_f32_16x16x32_bf16 v[118:121], v[194:197], v[222:225], v[118:121]
	v_mfma_f32_16x16x32_bf16 v[98:101], v[198:201], v[222:225], v[98:101]
	v_mfma_f32_16x16x32_bf16 v[74:77], v[202:205], v[222:225], v[74:77]
	s_waitcnt lgkmcnt(6)
	v_mfma_f32_16x16x32_bf16 v[110:113], v[178:181], v[226:229], v[110:113]
	v_mfma_f32_16x16x32_bf16 v[102:105], v[194:197], v[226:229], v[102:105]
	v_mfma_f32_16x16x32_bf16 v[82:85], v[198:201], v[226:229], v[82:85]
	v_mfma_f32_16x16x32_bf16 v[62:65], v[202:205], v[226:229], v[62:65]
	s_waitcnt lgkmcnt(5)
	v_mfma_f32_16x16x32_bf16 v[94:97], v[178:181], v[230:233], v[94:97]
	v_mfma_f32_16x16x32_bf16 v[86:89], v[194:197], v[230:233], v[86:89]
	v_mfma_f32_16x16x32_bf16 v[70:73], v[198:201], v[230:233], v[70:73]
	v_mfma_f32_16x16x32_bf16 v[54:57], v[202:205], v[230:233], v[54:57]
	s_waitcnt lgkmcnt(4)
	v_mfma_f32_16x16x32_bf16 v[78:81], v[178:181], v[234:237], v[78:81]
	v_mfma_f32_16x16x32_bf16 v[66:69], v[194:197], v[234:237], v[66:69]
	v_mfma_f32_16x16x32_bf16 v[58:61], v[198:201], v[234:237], v[58:61]
	v_mfma_f32_16x16x32_bf16 v[50:53], v[202:205], v[234:237], v[50:53]
	s_setprio 0
	s_waitcnt lgkmcnt(0)
	s_barrier
	s_add_i32 s20, s20, 1
	s_add_i32 s18, s18, 2
	v_add_u32_e32 v182, s19, v191
	v_add_u32_e32 v238, s19, v192
	ds_read_b128 v[178:181], v182 offset:32768
	ds_read_b128 v[194:197], v182 offset:34816
	ds_read_b128 v[198:201], v182 offset:36864
	ds_read_b128 v[202:205], v182 offset:38912
	ds_read_b128 v[206:209], v238
	ds_read_b128 v[210:213], v238 offset:2048
	ds_read_b128 v[214:217], v238 offset:4096
	ds_read_b128 v[218:221], v238 offset:6144
	ds_read_b128 v[222:225], v238 offset:8192
	ds_read_b128 v[226:229], v238 offset:10240
	ds_read_b128 v[230:233], v238 offset:12288
	ds_read_b128 v[234:237], v238 offset:14336
	s_min_u32 s21, s20, 29
	s_xor_b32 s19, s19, 0x10000
	v_add_u32_e32 v239, s19, v189
	s_waitcnt lgkmcnt(0)
	s_add_i32 s21, s21, 2
	s_barrier
	s_setprio 1
	s_waitcnt lgkmcnt(11)
	v_mfma_f32_16x16x32_bf16 v[174:177], v[178:181], v[206:209], v[174:177]
	s_lshl_b32 s22, s21, 1
	s_and_b32 s22, s22, 0x60
	s_add_i32 s22, s22, s12
	s_lshl_b32 s22, s22, 6
	v_mfma_f32_16x16x32_bf16 v[170:173], v[194:197], v[206:209], v[170:173]
	s_and_b32 s22, s22, 0x3f00
	s_or_b32 s22, s22, s13
	s_lshl_b32 s23, s21, 23
	s_lshl_b32 s22, s22, 9
	v_mfma_f32_16x16x32_bf16 v[158:161], v[198:201], v[206:209], v[158:161]
	s_and_b32 s23, s23, 0x7000000
	s_or_b32 s22, s22, s23
	s_lshl_b32 s23, s21, 8
	s_and_b32 s23, s23, 0x100
	s_or_b32 s22, s22, s23
	s_or_b32 s23, s22, 0x4000
	v_mfma_f32_16x16x32_bf16 v[142:145], v[202:205], v[206:209], v[142:145]
	s_waitcnt lgkmcnt(10)
	v_mfma_f32_16x16x32_bf16 v[166:169], v[178:181], v[210:213], v[166:169]
	v_mfma_f32_16x16x32_bf16 v[162:165], v[194:197], v[210:213], v[162:165]
	v_mfma_f32_16x16x32_bf16 v[146:149], v[198:201], v[210:213], v[146:149]
	s_or_b32 s23, s22, 0x8000
	v_mfma_f32_16x16x32_bf16 v[122:125], v[202:205], v[210:213], v[122:125]
	s_waitcnt lgkmcnt(9)
	v_mfma_f32_16x16x32_bf16 v[154:157], v[178:181], v[214:217], v[154:157]
	v_mfma_f32_16x16x32_bf16 v[150:153], v[194:197], v[214:217], v[150:153]
	v_mfma_f32_16x16x32_bf16 v[130:133], v[198:201], v[214:217], v[130:133]
	s_or_b32 s23, s22, 0xc000
	v_mfma_f32_16x16x32_bf16 v[106:109], v[202:205], v[214:217], v[106:109]
	s_waitcnt lgkmcnt(8)
	v_mfma_f32_16x16x32_bf16 v[138:141], v[178:181], v[218:221], v[138:141]
	v_mfma_f32_16x16x32_bf16 v[134:137], v[194:197], v[218:221], v[134:137]
	v_mfma_f32_16x16x32_bf16 v[114:117], v[198:201], v[218:221], v[114:117]
	s_or_b32 s23, s22, 0x10000
	v_mfma_f32_16x16x32_bf16 v[90:93], v[202:205], v[218:221], v[90:93]
	s_waitcnt lgkmcnt(7)
	v_mfma_f32_16x16x32_bf16 v[126:129], v[178:181], v[222:225], v[126:129]
	v_mfma_f32_16x16x32_bf16 v[118:121], v[194:197], v[222:225], v[118:121]
	v_mfma_f32_16x16x32_bf16 v[98:101], v[198:201], v[222:225], v[98:101]
	s_or_b32 s23, s22, 0x14000
	v_mfma_f32_16x16x32_bf16 v[74:77], v[202:205], v[222:225], v[74:77]
	s_waitcnt lgkmcnt(6)
	v_mfma_f32_16x16x32_bf16 v[110:113], v[178:181], v[226:229], v[110:113]
	v_mfma_f32_16x16x32_bf16 v[102:105], v[194:197], v[226:229], v[102:105]
	v_mfma_f32_16x16x32_bf16 v[82:85], v[198:201], v[226:229], v[82:85]
	s_or_b32 s27, s22, 0x18000
	s_or_b32 s28, s22, 0x1c000
	v_mfma_f32_16x16x32_bf16 v[62:65], v[202:205], v[226:229], v[62:65]
	s_waitcnt lgkmcnt(5)
	v_mfma_f32_16x16x32_bf16 v[94:97], v[178:181], v[230:233], v[94:97]
	v_mfma_f32_16x16x32_bf16 v[86:89], v[194:197], v[230:233], v[86:89]
	v_mfma_f32_16x16x32_bf16 v[70:73], v[198:201], v[230:233], v[70:73]
	v_mfma_f32_16x16x32_bf16 v[54:57], v[202:205], v[230:233], v[54:57]
	s_waitcnt lgkmcnt(4)
	v_mfma_f32_16x16x32_bf16 v[78:81], v[178:181], v[234:237], v[78:81]
	v_mfma_f32_16x16x32_bf16 v[66:69], v[194:197], v[234:237], v[66:69]
	v_mfma_f32_16x16x32_bf16 v[58:61], v[198:201], v[234:237], v[58:61]
	v_mfma_f32_16x16x32_bf16 v[50:53], v[202:205], v[234:237], v[50:53]
	s_setprio 0
	s_waitcnt lgkmcnt(0)
	s_barrier
	ds_read_b128 v[178:181], v182 offset:33792
	ds_read_b128 v[194:197], v182 offset:35840
	ds_read_b128 v[198:201], v182 offset:37888
	ds_read_b128 v[202:205], v182 offset:39936
	ds_read_b128 v[206:209], v238 offset:1024
	ds_read_b128 v[210:213], v238 offset:3072
	ds_read_b128 v[214:217], v238 offset:5120
	ds_read_b128 v[218:221], v238 offset:7168
	ds_read_b128 v[222:225], v238 offset:9216
	ds_read_b128 v[226:229], v238 offset:11264
	ds_read_b128 v[230:233], v238 offset:13312
	ds_read_b128 v[234:237], v238 offset:15360
	s_waitcnt lgkmcnt(0)
	s_barrier
	s_setprio 1
	s_waitcnt lgkmcnt(11)
	v_mfma_f32_16x16x32_bf16 v[174:177], v[178:181], v[206:209], v[174:177]
	s_lshl_b32 s21, s21, 7
	s_and_b32 s21, s21, 0x780
	s_or_b32 s21, s21, s14
	s_or_b32 s22, s21, 0x20000
	v_mfma_f32_16x16x32_bf16 v[170:173], v[194:197], v[206:209], v[170:173]
	v_mfma_f32_16x16x32_bf16 v[158:161], v[198:201], v[206:209], v[158:161]
	v_mfma_f32_16x16x32_bf16 v[142:145], v[202:205], v[206:209], v[142:145]
	s_waitcnt lgkmcnt(10)
	v_mfma_f32_16x16x32_bf16 v[166:169], v[178:181], v[210:213], v[166:169]
	v_mfma_f32_16x16x32_bf16 v[162:165], v[194:197], v[210:213], v[162:165]
	v_mfma_f32_16x16x32_bf16 v[146:149], v[198:201], v[210:213], v[146:149]
	v_mfma_f32_16x16x32_bf16 v[122:125], v[202:205], v[210:213], v[122:125]
	s_waitcnt lgkmcnt(9)
	v_mfma_f32_16x16x32_bf16 v[154:157], v[178:181], v[214:217], v[154:157]
	v_mfma_f32_16x16x32_bf16 v[150:153], v[194:197], v[214:217], v[150:153]
	v_mfma_f32_16x16x32_bf16 v[130:133], v[198:201], v[214:217], v[130:133]
	v_mfma_f32_16x16x32_bf16 v[106:109], v[202:205], v[214:217], v[106:109]
	s_waitcnt lgkmcnt(8)
	v_mfma_f32_16x16x32_bf16 v[138:141], v[178:181], v[218:221], v[138:141]
	v_mfma_f32_16x16x32_bf16 v[134:137], v[194:197], v[218:221], v[134:137]
	s_or_b32 s22, s21, 0x40000
	s_or_b32 s21, s21, 0x60000
	v_mfma_f32_16x16x32_bf16 v[114:117], v[198:201], v[218:221], v[114:117]
	v_mfma_f32_16x16x32_bf16 v[90:93], v[202:205], v[218:221], v[90:93]
	s_waitcnt lgkmcnt(7)
	v_mfma_f32_16x16x32_bf16 v[126:129], v[178:181], v[222:225], v[126:129]
	v_mfma_f32_16x16x32_bf16 v[118:121], v[194:197], v[222:225], v[118:121]
	v_mfma_f32_16x16x32_bf16 v[98:101], v[198:201], v[222:225], v[98:101]
	v_mfma_f32_16x16x32_bf16 v[74:77], v[202:205], v[222:225], v[74:77]
	s_waitcnt lgkmcnt(6)
	v_mfma_f32_16x16x32_bf16 v[110:113], v[178:181], v[226:229], v[110:113]
	v_mfma_f32_16x16x32_bf16 v[102:105], v[194:197], v[226:229], v[102:105]
	v_mfma_f32_16x16x32_bf16 v[82:85], v[198:201], v[226:229], v[82:85]
	v_mfma_f32_16x16x32_bf16 v[62:65], v[202:205], v[226:229], v[62:65]
	s_waitcnt lgkmcnt(5)
	v_mfma_f32_16x16x32_bf16 v[94:97], v[178:181], v[230:233], v[94:97]
	v_mfma_f32_16x16x32_bf16 v[86:89], v[194:197], v[230:233], v[86:89]
	v_mfma_f32_16x16x32_bf16 v[70:73], v[198:201], v[230:233], v[70:73]
	v_mfma_f32_16x16x32_bf16 v[54:57], v[202:205], v[230:233], v[54:57]
	s_waitcnt lgkmcnt(4)
	v_mfma_f32_16x16x32_bf16 v[78:81], v[178:181], v[234:237], v[78:81]
	v_mfma_f32_16x16x32_bf16 v[66:69], v[194:197], v[234:237], v[66:69]
	v_mfma_f32_16x16x32_bf16 v[58:61], v[198:201], v[234:237], v[58:61]
	v_mfma_f32_16x16x32_bf16 v[50:53], v[202:205], v[234:237], v[50:53]
	s_setprio 0
	s_and_b32 s21, s18, 32
	s_add_i32 s21, s21, s12
	s_lshl_b32 s21, s21, 6
	s_and_b32 s21, s21, 0x3f00
	v_add_lshl_u32 v182, v193, s21, 9
	v_lshl_add_u64 v[206:207], v[184:185], 0, v[182:183]
	v_add_co_u32_e32 v208, vcc, s8, v206
	s_nop 1
	v_addc_co_u32_e32 v209, vcc, 0, v207, vcc
	v_add_co_u32_e32 v210, vcc, s15, v206
	s_nop 1
	v_addc_co_u32_e32 v211, vcc, 0, v207, vcc
	v_add_co_u32_e32 v212, vcc, s9, v206
	s_nop 1
	v_addc_co_u32_e32 v213, vcc, 0, v207, vcc
	v_add_co_u32_e32 v214, vcc, s16, v206
	s_nop 1
	v_addc_co_u32_e32 v215, vcc, 0, v207, vcc
	v_add_co_u32_e32 v216, vcc, s10, v206
	s_nop 1
	v_addc_co_u32_e32 v217, vcc, 0, v207, vcc
	v_add_co_u32_e32 v218, vcc, s17, v206
	s_nop 1
	v_addc_co_u32_e32 v219, vcc, 0, v207, vcc
	v_add_co_u32_e32 v220, vcc, s11, v206
	s_nop 1
	v_addc_co_u32_e32 v221, vcc, 0, v207, vcc
	global_store_dwordx4 v[206:207], v[174:177], off
	global_store_dwordx4 v[206:207], v[170:173], off offset:64
	global_store_dwordx4 v[206:207], v[158:161], off offset:128
	global_store_dwordx4 v[206:207], v[142:145], off offset:192
	global_store_dwordx4 v[208:209], v[166:169], off
	global_store_dwordx4 v[208:209], v[162:165], off offset:64
	global_store_dwordx4 v[208:209], v[146:149], off offset:128
	global_store_dwordx4 v[208:209], v[122:125], off offset:192
	global_store_dwordx4 v[210:211], v[154:157], off
	global_store_dwordx4 v[210:211], v[150:153], off offset:64
	global_store_dwordx4 v[210:211], v[130:133], off offset:128
	global_store_dwordx4 v[210:211], v[106:109], off offset:192
	global_store_dwordx4 v[212:213], v[138:141], off
	global_store_dwordx4 v[212:213], v[134:137], off offset:64
	global_store_dwordx4 v[212:213], v[114:117], off offset:128
	global_store_dwordx4 v[212:213], v[90:93], off offset:192
	global_store_dwordx4 v[214:215], v[126:129], off
	global_store_dwordx4 v[214:215], v[118:121], off offset:64
	global_store_dwordx4 v[214:215], v[98:101], off offset:128
	global_store_dwordx4 v[214:215], v[74:77], off offset:192
	global_store_dwordx4 v[216:217], v[110:113], off
	global_store_dwordx4 v[216:217], v[102:105], off offset:64
	global_store_dwordx4 v[216:217], v[82:85], off offset:128
	global_store_dwordx4 v[216:217], v[62:65], off offset:192
	global_store_dwordx4 v[218:219], v[94:97], off
	global_store_dwordx4 v[218:219], v[86:89], off offset:64
	global_store_dwordx4 v[218:219], v[70:73], off offset:128
	global_store_dwordx4 v[218:219], v[54:57], off offset:192
	global_store_dwordx4 v[220:221], v[78:81], off
	global_store_dwordx4 v[220:221], v[66:69], off offset:64
	global_store_dwordx4 v[220:221], v[58:61], off offset:128
	global_store_dwordx4 v[220:221], v[50:53], off offset:192
	s_waitcnt lgkmcnt(0)
	s_barrier
	s_branch .LBB1_6
.Lfirst:
	v_add_u32_e32 v182, s19, v191
	v_add_u32_e32 v238, s19, v192
	ds_read_b128 v[178:181], v182 offset:32768
	ds_read_b128 v[194:197], v182 offset:34816
	ds_read_b128 v[198:201], v182 offset:36864
	ds_read_b128 v[202:205], v182 offset:38912
	ds_read_b128 v[206:209], v238
	ds_read_b128 v[210:213], v238 offset:2048
	ds_read_b128 v[214:217], v238 offset:4096
	ds_read_b128 v[218:221], v238 offset:6144
	ds_read_b128 v[222:225], v238 offset:8192
	ds_read_b128 v[226:229], v238 offset:10240
	ds_read_b128 v[230:233], v238 offset:12288
	ds_read_b128 v[234:237], v238 offset:14336
	s_min_u32 s21, s20, 29
	s_xor_b32 s19, s19, 0x10000
	v_add_u32_e32 v239, s19, v189
	s_waitcnt vmcnt(11)
	v_cvt_pk_bf16_f32 v13, v12, v13
	v_cvt_pk_bf16_f32 v12, v10, v11
	s_waitcnt vmcnt(10)
	v_cvt_pk_bf16_f32 v11, v20, v21
	v_cvt_pk_bf16_f32 v10, v18, v19
	ds_write2st64_b64 v239, v[12:13], v[10:11] offset1:8
	s_waitcnt vmcnt(9)
	v_cvt_pk_bf16_f32 v11, v24, v25
	v_cvt_pk_bf16_f32 v10, v22, v23
	s_waitcnt vmcnt(8)
	v_cvt_pk_bf16_f32 v13, v32, v33
	v_cvt_pk_bf16_f32 v12, v30, v31
	ds_write2st64_b64 v239, v[10:11], v[12:13] offset0:16 offset1:24
	s_waitcnt vmcnt(7)
	v_cvt_pk_bf16_f32 v11, v36, v37
	v_cvt_pk_bf16_f32 v10, v34, v35
	s_waitcnt vmcnt(6)
	v_cvt_pk_bf16_f32 v13, v40, v41
	v_cvt_pk_bf16_f32 v12, v38, v39
	ds_write2st64_b64 v239, v[10:11], v[12:13] offset0:32 offset1:40
	s_waitcnt lgkmcnt(0)
	s_add_i32 s21, s21, 2
	s_barrier
	s_setprio 1
	s_waitcnt lgkmcnt(11)
	v_mfma_f32_16x16x32_bf16 v[174:177], v[178:181], v[206:209], v[240:243]
	s_lshl_b32 s22, s21, 1
	s_and_b32 s22, s22, 0x60
	s_add_i32 s22, s22, s12
	s_lshl_b32 s22, s22, 6
	v_mfma_f32_16x16x32_bf16 v[170:173], v[194:197], v[206:209], v[244:247]
	s_and_b32 s22, s22, 0x3f00
	s_or_b32 s22, s22, s13
	s_lshl_b32 s23, s21, 23
	s_lshl_b32 s22, s22, 9
	v_mfma_f32_16x16x32_bf16 v[158:161], v[198:201], v[206:209], v[248:251]
	s_and_b32 s23, s23, 0x7000000
	s_or_b32 s22, s22, s23
	s_lshl_b32 s23, s21, 8
	s_and_b32 s23, s23, 0x100
	s_or_b32 s22, s22, s23
	s_or_b32 s23, s22, 0x4000
	buffer_load_dwordx4 v[10:13], v1, s[4:7], s22 offen sc0 nt
	v_mfma_f32_16x16x32_bf16 v[142:145], v[202:205], v[206:209], v[252:255]
	s_waitcnt lgkmcnt(10)
	v_mfma_f32_16x16x32_bf16 v[166:169], v[178:181], v[210:213], v[240:243]
	v_mfma_f32_16x16x32_bf16 v[162:165], v[194:197], v[210:213], v[244:247]
	v_mfma_f32_16x16x32_bf16 v[146:149], v[198:201], v[210:213], v[248:251]
	buffer_load_dwordx4 v[18:21], v1, s[4:7], s23 offen sc0 nt
	s_or_b32 s23, s22, 0x8000
	v_mfma_f32_16x16x32_bf16 v[122:125], v[202:205], v[210:213], v[252:255]
	s_waitcnt lgkmcnt(9)
	v_mfma_f32_16x16x32_bf16 v[154:157], v[178:181], v[214:217], v[240:243]
	v_mfma_f32_16x16x32_bf16 v[150:153], v[194:197], v[214:217], v[244:247]
	v_mfma_f32_16x16x32_bf16 v[130:133], v[198:201], v[214:217], v[248:251]
	buffer_load_dwordx4 v[22:25], v1, s[4:7], s23 offen sc0 nt
	s_or_b32 s23, s22, 0xc000
	v_mfma_f32_16x16x32_bf16 v[106:109], v[202:205], v[214:217], v[252:255]
	s_waitcnt lgkmcnt(8)
	v_mfma_f32_16x16x32_bf16 v[138:141], v[178:181], v[218:221], v[240:243]
	v_mfma_f32_16x16x32_bf16 v[134:137], v[194:197], v[218:221], v[244:247]
	v_mfma_f32_16x16x32_bf16 v[114:117], v[198:201], v[218:221], v[248:251]
	buffer_load_dwordx4 v[30:33], v1, s[4:7], s23 offen sc0 nt
	s_or_b32 s23, s22, 0x10000
	v_mfma_f32_16x16x32_bf16 v[90:93], v[202:205], v[218:221], v[252:255]
	s_waitcnt lgkmcnt(7)
	v_mfma_f32_16x16x32_bf16 v[126:129], v[178:181], v[222:225], v[240:243]
	v_mfma_f32_16x16x32_bf16 v[118:121], v[194:197], v[222:225], v[244:247]
	v_mfma_f32_16x16x32_bf16 v[98:101], v[198:201], v[222:225], v[248:251]
	buffer_load_dwordx4 v[34:37], v1, s[4:7], s23 offen sc0 nt
	s_or_b32 s23, s22, 0x14000
	v_mfma_f32_16x16x32_bf16 v[74:77], v[202:205], v[222:225], v[252:255]
	s_waitcnt lgkmcnt(6)
	v_mfma_f32_16x16x32_bf16 v[110:113], v[178:181], v[226:229], v[240:243]
	v_mfma_f32_16x16x32_bf16 v[102:105], v[194:197], v[226:229], v[244:247]
	v_mfma_f32_16x16x32_bf16 v[82:85], v[198:201], v[226:229], v[248:251]
	buffer_load_dwordx4 v[38:41], v1, s[4:7], s23 offen sc0 nt
	s_or_b32 s27, s22, 0x18000
	s_or_b32 s28, s22, 0x1c000
	v_mfma_f32_16x16x32_bf16 v[62:65], v[202:205], v[226:229], v[252:255]
	s_waitcnt lgkmcnt(5)
	v_mfma_f32_16x16x32_bf16 v[94:97], v[178:181], v[230:233], v[240:243]
	v_mfma_f32_16x16x32_bf16 v[86:89], v[194:197], v[230:233], v[244:247]
	v_mfma_f32_16x16x32_bf16 v[70:73], v[198:201], v[230:233], v[248:251]
	v_mfma_f32_16x16x32_bf16 v[54:57], v[202:205], v[230:233], v[252:255]
	s_waitcnt lgkmcnt(4)
	v_mfma_f32_16x16x32_bf16 v[78:81], v[178:181], v[234:237], v[240:243]
	v_mfma_f32_16x16x32_bf16 v[66:69], v[194:197], v[234:237], v[244:247]
	v_mfma_f32_16x16x32_bf16 v[58:61], v[198:201], v[234:237], v[248:251]
	v_mfma_f32_16x16x32_bf16 v[50:53], v[202:205], v[234:237], v[252:255]
	s_setprio 0
	s_waitcnt lgkmcnt(0)
	s_barrier
	ds_read_b128 v[178:181], v182 offset:33792
	ds_read_b128 v[194:197], v182 offset:35840
	ds_read_b128 v[198:201], v182 offset:37888
	ds_read_b128 v[202:205], v182 offset:39936
	ds_read_b128 v[206:209], v238 offset:1024
	ds_read_b128 v[210:213], v238 offset:3072
	ds_read_b128 v[214:217], v238 offset:5120
	ds_read_b128 v[218:221], v238 offset:7168
	ds_read_b128 v[222:225], v238 offset:9216
	ds_read_b128 v[226:229], v238 offset:11264
	ds_read_b128 v[230:233], v238 offset:13312
	ds_read_b128 v[234:237], v238 offset:15360
	v_add_u32_e32 v182, s19, v190
	s_waitcnt vmcnt(11)
	v_cvt_pk_bf16_f32 v42, v42, v43
	v_cvt_pk_bf16_f32 v43, v44, v45
	s_waitcnt vmcnt(9)
	v_cvt_pk_bf16_f32 v46, v46, v47
	v_cvt_pk_bf16_f32 v47, v48, v49
	ds_write2st64_b64 v239, v[42:43], v[46:47] offset0:48 offset1:56
	s_waitcnt vmcnt(9)
	ds_write_b128 v182, v[2:5] offset:32768
	s_waitcnt vmcnt(8)
	ds_write_b128 v182, v[6:9] offset:40960
	s_waitcnt vmcnt(7)
	ds_write_b128 v182, v[14:17] offset:49152
	s_waitcnt vmcnt(6)
	ds_write_b128 v182, v[26:29] offset:57344
	s_waitcnt lgkmcnt(0)
	s_barrier
	s_setprio 1
	s_waitcnt lgkmcnt(11)
	v_mfma_f32_16x16x32_bf16 v[174:177], v[178:181], v[206:209], v[174:177]
	s_lshl_b32 s21, s21, 7
	s_and_b32 s21, s21, 0x780
	s_or_b32 s21, s21, s14
	s_or_b32 s22, s21, 0x20000
	v_mfma_f32_16x16x32_bf16 v[170:173], v[194:197], v[206:209], v[170:173]
	v_mfma_f32_16x16x32_bf16 v[158:161], v[198:201], v[206:209], v[158:161]
	buffer_load_dwordx4 v[42:45], v1, s[4:7], s27 offen sc0 nt
	v_mfma_f32_16x16x32_bf16 v[142:145], v[202:205], v[206:209], v[142:145]
	s_waitcnt lgkmcnt(10)
	v_mfma_f32_16x16x32_bf16 v[166:169], v[178:181], v[210:213], v[166:169]
	v_mfma_f32_16x16x32_bf16 v[162:165], v[194:197], v[210:213], v[162:165]
	buffer_load_dwordx4 v[2:5], v188, s[0:3], s21 offen sc1
	v_mfma_f32_16x16x32_bf16 v[146:149], v[198:201], v[210:213], v[146:149]
	v_mfma_f32_16x16x32_bf16 v[122:125], v[202:205], v[210:213], v[122:125]
	s_waitcnt lgkmcnt(9)
	v_mfma_f32_16x16x32_bf16 v[154:157], v[178:181], v[214:217], v[154:157]
	v_mfma_f32_16x16x32_bf16 v[150:153], v[194:197], v[214:217], v[150:153]
	v_mfma_f32_16x16x32_bf16 v[130:133], v[198:201], v[214:217], v[130:133]
	buffer_load_dwordx4 v[46:49], v1, s[4:7], s28 offen sc0 nt
	v_mfma_f32_16x16x32_bf16 v[106:109], v[202:205], v[214:217], v[106:109]
	s_waitcnt lgkmcnt(8)
	v_mfma_f32_16x16x32_bf16 v[138:141], v[178:181], v[218:221], v[138:141]
	v_mfma_f32_16x16x32_bf16 v[134:137], v[194:197], v[218:221], v[134:137]
	buffer_load_dwordx4 v[6:9], v188, s[0:3], s22 offen sc1
	s_or_b32 s22, s21, 0x40000
	s_or_b32 s21, s21, 0x60000
	v_mfma_f32_16x16x32_bf16 v[114:117], v[198:201], v[218:221], v[114:117]
	v_mfma_f32_16x16x32_bf16 v[90:93], v[202:205], v[218:221], v[90:93]
	s_waitcnt lgkmcnt(7)
	v_mfma_f32_16x16x32_bf16 v[126:129], v[178:181], v[222:225], v[126:129]
	v_mfma_f32_16x16x32_bf16 v[118:121], v[194:197], v[222:225], v[118:121]
	v_mfma_f32_16x16x32_bf16 v[98:101], v[198:201], v[222:225], v[98:101]
	v_mfma_f32_16x16x32_bf16 v[74:77], v[202:205], v[222:225], v[74:77]
	s_waitcnt lgkmcnt(6)
	v_mfma_f32_16x16x32_bf16 v[110:113], v[178:181], v[226:229], v[110:113]
	v_mfma_f32_16x16x32_bf16 v[102:105], v[194:197], v[226:229], v[102:105]
	buffer_load_dwordx4 v[14:17], v188, s[0:3], s22 offen sc1
	v_mfma_f32_16x16x32_bf16 v[82:85], v[198:201], v[226:229], v[82:85]
	v_mfma_f32_16x16x32_bf16 v[62:65], v[202:205], v[226:229], v[62:65]
	s_waitcnt lgkmcnt(5)
	v_mfma_f32_16x16x32_bf16 v[94:97], v[178:181], v[230:233], v[94:97]
	v_mfma_f32_16x16x32_bf16 v[86:89], v[194:197], v[230:233], v[86:89]
	v_mfma_f32_16x16x32_bf16 v[70:73], v[198:201], v[230:233], v[70:73]
	v_mfma_f32_16x16x32_bf16 v[54:57], v[202:205], v[230:233], v[54:57]
	s_waitcnt lgkmcnt(4)
	v_mfma_f32_16x16x32_bf16 v[78:81], v[178:181], v[234:237], v[78:81]
	v_mfma_f32_16x16x32_bf16 v[66:69], v[194:197], v[234:237], v[66:69]
	buffer_load_dwordx4 v[26:29], v188, s[0:3], s21 offen sc1
	v_mfma_f32_16x16x32_bf16 v[58:61], v[198:201], v[234:237], v[58:61]
	v_mfma_f32_16x16x32_bf16 v[50:53], v[202:205], v[234:237], v[50:53]
	s_setprio 0
	s_branch .LBB1_3
